# speedup vs baseline: 1.0062x; 1.0062x over previous
.Lprep_go:
	s_lshl_b32 s27, s23, 12
	s_lshl_b32 s28, s22, 7
	s_add_i32 s27, s27, s28
	s_add_u32 s0, s0, s27
	s_addc_u32 s1, s1, 0
	global_load_dwordx4 v[8:11], v3, s[0:1] sc1 nt
	global_load_dwordx4 v[12:15], v3, s[0:1] offset:16 sc1 nt
	global_load_dwordx4 v[16:19], v3, s[0:1] offset:128 sc1 nt
	global_load_dwordx4 v[20:23], v3, s[0:1] offset:144 sc1 nt
	global_load_dwordx4 v[24:27], v3, s[0:1] offset:256 sc1 nt
	global_load_dwordx4 v[28:31], v3, s[0:1] offset:272 sc1 nt
	global_load_dwordx4 v[32:35], v3, s[0:1] offset:384 sc1 nt
	global_load_dwordx4 v[36:39], v3, s[0:1] offset:400 sc1 nt
	s_mul_i32 s27, s22, s25
	s_lshl_b32 s28, s24, 6
	s_add_i32 s27, s27, s28
	s_add_u32 s2, s2, s27
	s_addc_u32 s3, s3, 0
	s_add_u32 s4, s2, s25
	s_addc_u32 s5, s3, 0
	s_add_u32 s6, s4, s25
	s_addc_u32 s7, s5, 0
	s_add_u32 s8, s6, s25
	s_addc_u32 s9, s7, 0
	s_waitcnt vmcnt(6)
	v_cvt_pk_f16_f32 v8, v8, v9
	v_cvt_pk_f16_f32 v9, v10, v11
	v_cvt_pk_f16_f32 v10, v12, v13
	v_cvt_pk_f16_f32 v11, v14, v15
	global_store_dwordx4 v4, v[8:11], s[2:3] sc1
	s_waitcnt vmcnt(5)
	v_cvt_pk_f16_f32 v16, v16, v17
	v_cvt_pk_f16_f32 v17, v18, v19
	v_cvt_pk_f16_f32 v18, v20, v21
	v_cvt_pk_f16_f32 v19, v22, v23
	global_store_dwordx4 v4, v[16:19], s[4:5] sc1
	s_waitcnt vmcnt(4)
	v_cvt_pk_f16_f32 v24, v24, v25
	v_cvt_pk_f16_f32 v25, v26, v27
	v_cvt_pk_f16_f32 v26, v28, v29
	v_cvt_pk_f16_f32 v27, v30, v31
	global_store_dwordx4 v4, v[24:27], s[6:7] sc1
	s_waitcnt vmcnt(3)
	v_cvt_pk_f16_f32 v32, v32, v33
	v_cvt_pk_f16_f32 v33, v34, v35
	v_cvt_pk_f16_f32 v34, v36, v37
	v_cvt_pk_f16_f32 v35, v38, v39
	global_store_dwordx4 v4, v[32:35], s[8:9] sc1
	s_endpgm
